# baseline (speedup 1.0000x reference)
_Z11prep_kernelPKfS0_S0_S0_S0_S0_S0_S0_S0_PKiPDv8_DF16bS4_PfS5_S5_PiPt:
	s_load_dwordx4 s[16:19], s[0:1], 0x0
	s_load_dwordx4 s[20:23], s[0:1], 0x10
	s_load_dwordx4 s[24:27], s[0:1], 0x20
	s_load_dwordx4 s[28:31], s[0:1], 0x30
	s_load_dwordx4 s[32:35], s[0:1], 0x40
	s_load_dwordx2 s[36:37], s[0:1], 0x80
	v_and_b32_e32 v126, 63, v0
	v_lshrrev_b32_e32 v128, 6, v0
	v_and_b32_e32 v1, 15, v0
	v_bfe_u32 v24, v0, 4, 2
	v_lshl_or_b32 v107, v128, 4, v1
	v_lshlrev_b32_e32 v106, 2, v107
	v_lshlrev_b32_e32 v127, 2, v0
	v_lshlrev_b32_e32 v25, 1, v107
	v_and_b32_e32 v26, 48, v0
	v_mul_u32_u24_e32 v27, 0x440, v24
	v_lshlrev_b32_e32 v120, 4, v0
	v_lshrrev_b32_e32 v58, 5, v0
	v_mul_u32_u24_e32 v58, 0x110, v58
	v_and_b32_e32 v125, 31, v0
	v_lshl_add_u32 v58, v125, 3, v58
	v_add_u32_e32 v124, 0x1b400, v58
	v_mul_u32_u24_e32 v52, 0x110, v1
	v_add_u32_e32 v52, v52, v26
	v_add_u32_e32 v53, 0x1b400, v52
	v_add_u32_e32 v54, 0x1c500, v52
	v_add_u32_e32 v55, v27, v25
	v_add_u32_e32 v55, 0x1c500, v55
	v_mul_u32_u24_e32 v56, 0x110, v107
	v_add_u32_e32 v56, v56, v26
	v_add_u32_e32 v57, 0x8800, v56
	s_lshl_b32 s12, s2, 4
	s_add_i32 s3, s12, 0xfffff800
	s_cmpk_gt_i32 s2, 0x7f
	s_cselect_b64 s[6:7], -1, 0
	s_mov_b32 s48, 0
	s_mov_b32 s49, -1
	v_lshl_or_b32 v123, s2, 3, v128
	v_lshlrev_b32_e32 v123, 12, v123
	v_lshl_add_u32 v123, v126, 4, v123
	s_waitcnt lgkmcnt(0)
	s_sub_i32 s13, s2, 64
	s_cmp_lt_u32 s13, 64
	s_cbranch_scc1 .Lp_mask
	s_lshl_b32 s15, s2, 5
	s_cmpk_lt_i32 s2, 0x80
	s_cselect_b32 s38, s16, s18
	s_cselect_b32 s39, s17, s19
	s_cselect_b32 s40, s20, s24
	s_cselect_b32 s41, s21, s25
	s_cselect_b32 s13, s15, s3
	s_cselect_b32 s44, 0x3db504f3, 1.0
	s_lshl_b32 s13, s13, 9
	s_add_u32 s38, s38, s13
	s_addc_u32 s39, s39, 0
	global_load_dwordx4 v[2:5], v120, s[38:39] nt
	s_and_b32 s13, s2, 7
	s_lshl_b32 s14, s13, 13
	v_add_u32_e32 v125, s14, v120
	global_load_dwordx4 v[80:83], v125, s[40:41]
	s_add_i32 s13, s2, 1
	s_and_b32 s13, s13, 7
	s_lshl_b32 s14, s13, 13
	v_add_u32_e32 v125, s14, v120
	global_load_dwordx4 v[84:87], v125, s[40:41]
	s_add_i32 s13, s2, 2
	s_and_b32 s13, s13, 7
	s_lshl_b32 s14, s13, 13
	v_add_u32_e32 v125, s14, v120
	global_load_dwordx4 v[88:91], v125, s[40:41]
	s_add_i32 s13, s2, 3
	s_and_b32 s13, s13, 7
	s_lshl_b32 s14, s13, 13
	v_add_u32_e32 v125, s14, v120
	global_load_dwordx4 v[92:95], v125, s[40:41]
	s_add_i32 s13, s2, 4
	s_and_b32 s13, s13, 7
	s_lshl_b32 s14, s13, 13
	v_add_u32_e32 v125, s14, v120
	global_load_dwordx4 v[96:99], v125, s[40:41]
	s_add_i32 s13, s2, 5
	s_and_b32 s13, s13, 7
	s_lshl_b32 s14, s13, 13
	v_add_u32_e32 v125, s14, v120
	global_load_dwordx4 v[100:103], v125, s[40:41]
	s_add_i32 s13, s2, 6
	s_and_b32 s13, s13, 7
	s_lshl_b32 s14, s13, 13
	v_add_u32_e32 v125, s14, v120
	global_load_dwordx4 v[108:111], v125, s[40:41]
	s_add_i32 s13, s2, 7
	s_and_b32 s13, s13, 7
	s_lshl_b32 s14, s13, 13
	v_add_u32_e32 v125, s14, v120
	global_load_dwordx4 v[112:115], v125, s[40:41]
	global_load_dword v129, v106, s[32:33]
	global_load_dword v130, v106, s[30:31]
	s_and_b64 vcc, exec, s[6:7]
	s_cbranch_vccz .Lp_q
	v_cmp_gt_u32_e32 vcc, 32, v126
	v_mov_b32_e32 v198, 0x3db504f3
	v_mov_b32_e32 v125, s22
	v_mov_b32_e32 v104, s26
	v_cndmask_b32_e32 v198, 1.0, v198, vcc
	v_cndmask_b32_e32 v104, v104, v125, vcc
	v_mov_b32_e32 v125, s23
	v_mov_b32_e32 v105, s27
	v_cndmask_b32_e32 v105, v105, v125, vcc
	v_and_b32_e32 v196, 31, v126
	v_lshlrev_b32_e32 v196, 4, v196
	v_mov_b32_e32 v197, 0
	v_lshl_add_u64 v[104:105], v[104:105], 0, v[196:197]
	global_load_dwordx4 v[116:119], v[104:105], off
	v_lshlrev_b32_e32 v121, 14, v128
	v_lshl_add_u32 v121, v126, 4, v121
	s_and_b32 s13, s2, 15
	s_lshl_b32 s14, s13, 10
	s_add_u32 s46, s28, s14
	s_addc_u32 s47, s29, 0
	global_load_dwordx4 v[132:135], v121, s[46:47]
	s_add_i32 s13, s2, 1
	s_and_b32 s13, s13, 15
	s_lshl_b32 s14, s13, 10
	s_add_u32 s46, s28, s14
	s_addc_u32 s47, s29, 0
	global_load_dwordx4 v[136:139], v121, s[46:47]
	s_add_i32 s13, s2, 2
	s_and_b32 s13, s13, 15
	s_lshl_b32 s14, s13, 10
	s_add_u32 s46, s28, s14
	s_addc_u32 s47, s29, 0
	global_load_dwordx4 v[140:143], v121, s[46:47]
	s_add_i32 s13, s2, 3
	s_and_b32 s13, s13, 15
	s_lshl_b32 s14, s13, 10
	s_add_u32 s46, s28, s14
	s_addc_u32 s47, s29, 0
	global_load_dwordx4 v[144:147], v121, s[46:47]
	s_add_i32 s13, s2, 4
	s_and_b32 s13, s13, 15
	s_lshl_b32 s14, s13, 10
	s_add_u32 s46, s28, s14
	s_addc_u32 s47, s29, 0
	global_load_dwordx4 v[148:151], v121, s[46:47]
	s_add_i32 s13, s2, 5
	s_and_b32 s13, s13, 15
	s_lshl_b32 s14, s13, 10
	s_add_u32 s46, s28, s14
	s_addc_u32 s47, s29, 0
	global_load_dwordx4 v[152:155], v121, s[46:47]
	s_add_i32 s13, s2, 6
	s_and_b32 s13, s13, 15
	s_lshl_b32 s14, s13, 10
	s_add_u32 s46, s28, s14
	s_addc_u32 s47, s29, 0
	global_load_dwordx4 v[156:159], v121, s[46:47]
	s_add_i32 s13, s2, 7
	s_and_b32 s13, s13, 15
	s_lshl_b32 s14, s13, 10
	s_add_u32 s46, s28, s14
	s_addc_u32 s47, s29, 0
	global_load_dwordx4 v[160:163], v121, s[46:47]
	s_add_i32 s13, s2, 8
	s_and_b32 s13, s13, 15
	s_lshl_b32 s14, s13, 10
	s_add_u32 s46, s28, s14
	s_addc_u32 s47, s29, 0
	global_load_dwordx4 v[164:167], v121, s[46:47]
	s_add_i32 s13, s2, 9
	s_and_b32 s13, s13, 15
	s_lshl_b32 s14, s13, 10
	s_add_u32 s46, s28, s14
	s_addc_u32 s47, s29, 0
	global_load_dwordx4 v[168:171], v121, s[46:47]
	s_add_i32 s13, s2, 10
	s_and_b32 s13, s13, 15
	s_lshl_b32 s14, s13, 10
	s_add_u32 s46, s28, s14
	s_addc_u32 s47, s29, 0
	global_load_dwordx4 v[172:175], v121, s[46:47]
	s_add_i32 s13, s2, 11
	s_and_b32 s13, s13, 15
	s_lshl_b32 s14, s13, 10
	s_add_u32 s46, s28, s14
	s_addc_u32 s47, s29, 0
	global_load_dwordx4 v[176:179], v121, s[46:47]
	s_add_i32 s13, s2, 12
	s_and_b32 s13, s13, 15
	s_lshl_b32 s14, s13, 10
	s_add_u32 s46, s28, s14
	s_addc_u32 s47, s29, 0
	global_load_dwordx4 v[180:183], v121, s[46:47]
	s_add_i32 s13, s2, 13
	s_and_b32 s13, s13, 15
	s_lshl_b32 s14, s13, 10
	s_add_u32 s46, s28, s14
	s_addc_u32 s47, s29, 0
	global_load_dwordx4 v[184:187], v121, s[46:47]
	s_add_i32 s13, s2, 14
	s_and_b32 s13, s13, 15
	s_lshl_b32 s14, s13, 10
	s_add_u32 s46, s28, s14
	s_addc_u32 s47, s29, 0
	global_load_dwordx4 v[188:191], v121, s[46:47]
	s_add_i32 s13, s2, 15
	s_and_b32 s13, s13, 15
	s_lshl_b32 s14, s13, 10
	s_add_u32 s46, s28, s14
	s_addc_u32 s47, s29, 0
	global_load_dwordx4 v[192:195], v121, s[46:47]
	v_mul_u32_u24_e32 v59, 0x1040, v128
	v_lshl_add_u32 v59, v126, 2, v59
	v_add_u32_e32 v59, 0x11000, v59
	v_mul_u32_u24_e32 v76, 0x1100, v128
	v_lshl_add_u32 v76, v126, 3, v76
	v_add_u32_e32 v76, 0x8700, v76
	v_lshrrev_b32_e32 v77, 2, v126
	v_mul_u32_u24_e32 v77, 0x104, v77
	v_mul_u32_u24_e32 v125, 0x1040, v128
	v_add_u32_e32 v77, v77, v125
	v_and_b32_e32 v125, 3, v126
	v_lshl_add_u32 v77, v125, 6, v77
	v_add_u32_e32 v77, 0x11000, v77
	s_waitcnt vmcnt(27)
	v_cvt_pk_bf16_f32 v12, v2, v3
	v_cvt_pk_bf16_f32 v13, v4, v5
	ds_write_b64 v124, v[12:13]
	s_waitcnt vmcnt(26)
	v_cvt_pk_bf16_f32 v6, v80, v81
	v_cvt_pk_bf16_f32 v7, v82, v83
	s_and_b32 s13, s2, 7
	s_mul_i32 s14, s13, 0x1100
	v_add_u32_e32 v125, s14, v58
	ds_write_b64 v125, v[6:7]
	s_waitcnt vmcnt(25)
	v_cvt_pk_bf16_f32 v8, v84, v85
	v_cvt_pk_bf16_f32 v9, v86, v87
	s_add_i32 s13, s2, 1
	s_and_b32 s13, s13, 7
	s_mul_i32 s14, s13, 0x1100
	v_add_u32_e32 v10, s14, v58
	ds_write_b64 v10, v[8:9]
	s_waitcnt vmcnt(24)
	v_cvt_pk_bf16_f32 v6, v88, v89
	v_cvt_pk_bf16_f32 v7, v90, v91
	s_add_i32 s13, s2, 2
	s_and_b32 s13, s13, 7
	s_mul_i32 s14, s13, 0x1100
	v_add_u32_e32 v125, s14, v58
	ds_write_b64 v125, v[6:7]
	s_waitcnt vmcnt(23)
	v_cvt_pk_bf16_f32 v8, v92, v93
	v_cvt_pk_bf16_f32 v9, v94, v95
	s_add_i32 s13, s2, 3
	s_and_b32 s13, s13, 7
	s_mul_i32 s14, s13, 0x1100
	v_add_u32_e32 v10, s14, v58
	ds_write_b64 v10, v[8:9]
	s_waitcnt vmcnt(22)
	v_cvt_pk_bf16_f32 v6, v96, v97
	v_cvt_pk_bf16_f32 v7, v98, v99
	s_add_i32 s13, s2, 4
	s_and_b32 s13, s13, 7
	s_mul_i32 s14, s13, 0x1100
	v_add_u32_e32 v125, s14, v58
	ds_write_b64 v125, v[6:7]
	s_waitcnt vmcnt(21)
	v_cvt_pk_bf16_f32 v8, v100, v101
	v_cvt_pk_bf16_f32 v9, v102, v103
	s_add_i32 s13, s2, 5
	s_and_b32 s13, s13, 7
	s_mul_i32 s14, s13, 0x1100
	v_add_u32_e32 v10, s14, v58
	ds_write_b64 v10, v[8:9]
	s_waitcnt vmcnt(20)
	v_cvt_pk_bf16_f32 v6, v108, v109
	v_cvt_pk_bf16_f32 v7, v110, v111
	s_add_i32 s13, s2, 6
	s_and_b32 s13, s13, 7
	s_mul_i32 s14, s13, 0x1100
	v_add_u32_e32 v125, s14, v58
	ds_write_b64 v125, v[6:7]
	s_waitcnt vmcnt(19)
	v_cvt_pk_bf16_f32 v8, v112, v113
	v_cvt_pk_bf16_f32 v9, v114, v115
	s_add_i32 s13, s2, 7
	s_and_b32 s13, s13, 7
	s_mul_i32 s14, s13, 0x1100
	v_add_u32_e32 v10, s14, v58
	ds_write_b64 v10, v[8:9]
	s_waitcnt vmcnt(16)
	v_pk_mul_f32 v[116:117], v[198:199], v[116:117] op_sel_hi:[0,1]
	v_pk_mul_f32 v[118:119], v[198:199], v[118:119] op_sel_hi:[0,1]
	s_waitcnt vmcnt(15)
	v_mul_f32_e32 v6, v117, v133
	v_mul_f32_e32 v7, v119, v135
	v_fmac_f32_e32 v6, v116, v132
	v_fmac_f32_e32 v7, v118, v134
	s_and_b32 s13, s2, 15
	s_mul_i32 s14, s13, 0x104
	s_mul_i32 s15, s13, 0x110
	v_add_f32_e32 v6, v6, v7
	v_add_u32_e32 v125, s14, v59
	ds_write_b32 v125, v6
	v_cvt_pk_bf16_f32 v8, v132, v133
	v_cvt_pk_bf16_f32 v9, v134, v135
	v_add_u32_e32 v10, s15, v76
	s_mov_b64 exec, s[48:49]
	ds_write_b64 v10, v[8:9]
	s_mov_b64 exec, -1
	s_waitcnt vmcnt(14)
	v_mul_f32_e32 v11, v117, v137
	v_mul_f32_e32 v15, v119, v139
	v_fmac_f32_e32 v11, v116, v136
	v_fmac_f32_e32 v15, v118, v138
	s_add_i32 s13, s2, 1
	s_and_b32 s13, s13, 15
	s_mul_i32 s14, s13, 0x104
	s_mul_i32 s15, s13, 0x110
	v_add_f32_e32 v11, v11, v15
	v_add_u32_e32 v16, s14, v59
	ds_write_b32 v16, v11
	v_cvt_pk_bf16_f32 v12, v136, v137
	v_cvt_pk_bf16_f32 v13, v138, v139
	v_add_u32_e32 v14, s15, v76
	s_mov_b64 exec, s[48:49]
	ds_write_b64 v14, v[12:13]
	s_mov_b64 exec, -1
	s_waitcnt vmcnt(13)
	v_mul_f32_e32 v6, v117, v141
	v_mul_f32_e32 v7, v119, v143
	v_fmac_f32_e32 v6, v116, v140
	v_fmac_f32_e32 v7, v118, v142
	s_add_i32 s13, s2, 2
	s_and_b32 s13, s13, 15
	s_mul_i32 s14, s13, 0x104
	s_mul_i32 s15, s13, 0x110
	v_add_f32_e32 v6, v6, v7
	v_add_u32_e32 v125, s14, v59
	ds_write_b32 v125, v6
	v_cvt_pk_bf16_f32 v8, v140, v141
	v_cvt_pk_bf16_f32 v9, v142, v143
	v_add_u32_e32 v10, s15, v76
	s_mov_b64 exec, s[48:49]
	ds_write_b64 v10, v[8:9]
	s_mov_b64 exec, -1
	s_waitcnt vmcnt(12)
	v_mul_f32_e32 v11, v117, v145
	v_mul_f32_e32 v15, v119, v147
	v_fmac_f32_e32 v11, v116, v144
	v_fmac_f32_e32 v15, v118, v146
	s_add_i32 s13, s2, 3
	s_and_b32 s13, s13, 15
	s_mul_i32 s14, s13, 0x104
	s_mul_i32 s15, s13, 0x110
	v_add_f32_e32 v11, v11, v15
	v_add_u32_e32 v16, s14, v59
	ds_write_b32 v16, v11
	v_cvt_pk_bf16_f32 v12, v144, v145
	v_cvt_pk_bf16_f32 v13, v146, v147
	v_add_u32_e32 v14, s15, v76
	s_mov_b64 exec, s[48:49]
	ds_write_b64 v14, v[12:13]
	s_mov_b64 exec, -1
	s_waitcnt vmcnt(11)
	v_mul_f32_e32 v6, v117, v149
	v_mul_f32_e32 v7, v119, v151
	v_fmac_f32_e32 v6, v116, v148
	v_fmac_f32_e32 v7, v118, v150
	s_add_i32 s13, s2, 4
	s_and_b32 s13, s13, 15
	s_mul_i32 s14, s13, 0x104
	s_mul_i32 s15, s13, 0x110
	v_add_f32_e32 v6, v6, v7
	v_add_u32_e32 v125, s14, v59
	ds_write_b32 v125, v6
	v_cvt_pk_bf16_f32 v8, v148, v149
	v_cvt_pk_bf16_f32 v9, v150, v151
	v_add_u32_e32 v10, s15, v76
	s_mov_b64 exec, s[48:49]
	ds_write_b64 v10, v[8:9]
	s_mov_b64 exec, -1
	s_waitcnt vmcnt(10)
	v_mul_f32_e32 v11, v117, v153
	v_mul_f32_e32 v15, v119, v155
	v_fmac_f32_e32 v11, v116, v152
	v_fmac_f32_e32 v15, v118, v154
	s_add_i32 s13, s2, 5
	s_and_b32 s13, s13, 15
	s_mul_i32 s14, s13, 0x104
	s_mul_i32 s15, s13, 0x110
	v_add_f32_e32 v11, v11, v15
	v_add_u32_e32 v16, s14, v59
	ds_write_b32 v16, v11
	v_cvt_pk_bf16_f32 v12, v152, v153
	v_cvt_pk_bf16_f32 v13, v154, v155
	v_add_u32_e32 v14, s15, v76
	s_mov_b64 exec, s[48:49]
	ds_write_b64 v14, v[12:13]
	s_mov_b64 exec, -1
	s_waitcnt vmcnt(9)
	v_mul_f32_e32 v6, v117, v157
	v_mul_f32_e32 v7, v119, v159
	v_fmac_f32_e32 v6, v116, v156
	v_fmac_f32_e32 v7, v118, v158
	s_add_i32 s13, s2, 6
	s_and_b32 s13, s13, 15
	s_mul_i32 s14, s13, 0x104
	s_mul_i32 s15, s13, 0x110
	v_add_f32_e32 v6, v6, v7
	v_add_u32_e32 v125, s14, v59
	ds_write_b32 v125, v6
	v_cvt_pk_bf16_f32 v8, v156, v157
	v_cvt_pk_bf16_f32 v9, v158, v159
	v_add_u32_e32 v10, s15, v76
	s_mov_b64 exec, s[48:49]
	ds_write_b64 v10, v[8:9]
	s_mov_b64 exec, -1
	s_waitcnt vmcnt(8)
	v_mul_f32_e32 v11, v117, v161
	v_mul_f32_e32 v15, v119, v163
	v_fmac_f32_e32 v11, v116, v160
	v_fmac_f32_e32 v15, v118, v162
	s_add_i32 s13, s2, 7
	s_and_b32 s13, s13, 15
	s_mul_i32 s14, s13, 0x104
	s_mul_i32 s15, s13, 0x110
	v_add_f32_e32 v11, v11, v15
	v_add_u32_e32 v16, s14, v59
	ds_write_b32 v16, v11
	v_cvt_pk_bf16_f32 v12, v160, v161
	v_cvt_pk_bf16_f32 v13, v162, v163
	v_add_u32_e32 v14, s15, v76
	s_mov_b64 exec, s[48:49]
	ds_write_b64 v14, v[12:13]
	s_mov_b64 exec, -1
	s_waitcnt vmcnt(7)
	v_mul_f32_e32 v6, v117, v165
	v_mul_f32_e32 v7, v119, v167
	v_fmac_f32_e32 v6, v116, v164
	v_fmac_f32_e32 v7, v118, v166
	s_add_i32 s13, s2, 8
	s_and_b32 s13, s13, 15
	s_mul_i32 s14, s13, 0x104
	s_mul_i32 s15, s13, 0x110
	v_add_f32_e32 v6, v6, v7
	v_add_u32_e32 v125, s14, v59
	ds_write_b32 v125, v6
	v_cvt_pk_bf16_f32 v8, v164, v165
	v_cvt_pk_bf16_f32 v9, v166, v167
	v_add_u32_e32 v10, s15, v76
	s_mov_b64 exec, s[48:49]
	ds_write_b64 v10, v[8:9]
	s_mov_b64 exec, -1
	s_waitcnt vmcnt(6)
	v_mul_f32_e32 v11, v117, v169
	v_mul_f32_e32 v15, v119, v171
	v_fmac_f32_e32 v11, v116, v168
	v_fmac_f32_e32 v15, v118, v170
	s_add_i32 s13, s2, 9
	s_and_b32 s13, s13, 15
	s_mul_i32 s14, s13, 0x104
	s_mul_i32 s15, s13, 0x110
	v_add_f32_e32 v11, v11, v15
	v_add_u32_e32 v16, s14, v59
	ds_write_b32 v16, v11
	v_cvt_pk_bf16_f32 v12, v168, v169
	v_cvt_pk_bf16_f32 v13, v170, v171
	v_add_u32_e32 v14, s15, v76
	s_mov_b64 exec, s[48:49]
	ds_write_b64 v14, v[12:13]
	s_mov_b64 exec, -1
	s_waitcnt vmcnt(5)
	v_mul_f32_e32 v6, v117, v173
	v_mul_f32_e32 v7, v119, v175
	v_fmac_f32_e32 v6, v116, v172
	v_fmac_f32_e32 v7, v118, v174
	s_add_i32 s13, s2, 10
	s_and_b32 s13, s13, 15
	s_mul_i32 s14, s13, 0x104
	s_mul_i32 s15, s13, 0x110
	v_add_f32_e32 v6, v6, v7
	v_add_u32_e32 v125, s14, v59
	ds_write_b32 v125, v6
	v_cvt_pk_bf16_f32 v8, v172, v173
	v_cvt_pk_bf16_f32 v9, v174, v175
	v_add_u32_e32 v10, s15, v76
	s_mov_b64 exec, s[48:49]
	ds_write_b64 v10, v[8:9]
	s_mov_b64 exec, -1
	s_waitcnt vmcnt(4)
	v_mul_f32_e32 v11, v117, v177
	v_mul_f32_e32 v15, v119, v179
	v_fmac_f32_e32 v11, v116, v176
	v_fmac_f32_e32 v15, v118, v178
	s_add_i32 s13, s2, 11
	s_and_b32 s13, s13, 15
	s_mul_i32 s14, s13, 0x104
	s_mul_i32 s15, s13, 0x110
	v_add_f32_e32 v11, v11, v15
	v_add_u32_e32 v16, s14, v59
	ds_write_b32 v16, v11
	v_cvt_pk_bf16_f32 v12, v176, v177
	v_cvt_pk_bf16_f32 v13, v178, v179
	v_add_u32_e32 v14, s15, v76
	s_mov_b64 exec, s[48:49]
	ds_write_b64 v14, v[12:13]
	s_mov_b64 exec, -1
	s_waitcnt vmcnt(3)
	v_mul_f32_e32 v6, v117, v181
	v_mul_f32_e32 v7, v119, v183
	v_fmac_f32_e32 v6, v116, v180
	v_fmac_f32_e32 v7, v118, v182
	s_add_i32 s13, s2, 12
	s_and_b32 s13, s13, 15
	s_mul_i32 s14, s13, 0x104
	s_mul_i32 s15, s13, 0x110
	v_add_f32_e32 v6, v6, v7
	v_add_u32_e32 v125, s14, v59
	ds_write_b32 v125, v6
	v_cvt_pk_bf16_f32 v8, v180, v181
	v_cvt_pk_bf16_f32 v9, v182, v183
	v_add_u32_e32 v10, s15, v76
	s_mov_b64 exec, s[48:49]
	ds_write_b64 v10, v[8:9]
	s_mov_b64 exec, -1
	s_waitcnt vmcnt(2)
	v_mul_f32_e32 v11, v117, v185
	v_mul_f32_e32 v15, v119, v187
	v_fmac_f32_e32 v11, v116, v184
	v_fmac_f32_e32 v15, v118, v186
	s_add_i32 s13, s2, 13
	s_and_b32 s13, s13, 15
	s_mul_i32 s14, s13, 0x104
	s_mul_i32 s15, s13, 0x110
	v_add_f32_e32 v11, v11, v15
	v_add_u32_e32 v16, s14, v59
	ds_write_b32 v16, v11
	v_cvt_pk_bf16_f32 v12, v184, v185
	v_cvt_pk_bf16_f32 v13, v186, v187
	v_add_u32_e32 v14, s15, v76
	s_mov_b64 exec, s[48:49]
	ds_write_b64 v14, v[12:13]
	s_mov_b64 exec, -1
	s_waitcnt vmcnt(1)
	v_mul_f32_e32 v6, v117, v189
	v_mul_f32_e32 v7, v119, v191
	v_fmac_f32_e32 v6, v116, v188
	v_fmac_f32_e32 v7, v118, v190
	s_add_i32 s13, s2, 14
	s_and_b32 s13, s13, 15
	s_mul_i32 s14, s13, 0x104
	s_mul_i32 s15, s13, 0x110
	v_add_f32_e32 v6, v6, v7
	v_add_u32_e32 v125, s14, v59
	ds_write_b32 v125, v6
	v_cvt_pk_bf16_f32 v8, v188, v189
	v_cvt_pk_bf16_f32 v9, v190, v191
	v_add_u32_e32 v10, s15, v76
	s_mov_b64 exec, s[48:49]
	ds_write_b64 v10, v[8:9]
	s_mov_b64 exec, -1
	s_waitcnt vmcnt(0)
	v_mul_f32_e32 v11, v117, v193
	v_mul_f32_e32 v15, v119, v195
	v_fmac_f32_e32 v11, v116, v192
	v_fmac_f32_e32 v15, v118, v194
	s_add_i32 s13, s2, 15
	s_and_b32 s13, s13, 15
	s_mul_i32 s14, s13, 0x104
	s_mul_i32 s15, s13, 0x110
	v_add_f32_e32 v11, v11, v15
	v_add_u32_e32 v16, s14, v59
	ds_write_b32 v16, v11
	v_cvt_pk_bf16_f32 v12, v192, v193
	v_cvt_pk_bf16_f32 v13, v194, v195
	v_add_u32_e32 v14, s15, v76
	s_mov_b64 exec, s[48:49]
	ds_write_b64 v14, v[12:13]
	s_mov_b64 exec, -1
	s_waitcnt lgkmcnt(0)
	ds_read2_b32 v[60:61], v77 offset0:0 offset1:1
	ds_read2_b32 v[62:63], v77 offset0:2 offset1:3
	ds_read2_b32 v[64:65], v77 offset0:4 offset1:5
	ds_read2_b32 v[66:67], v77 offset0:6 offset1:7
	ds_read2_b32 v[68:69], v77 offset0:8 offset1:9
	ds_read2_b32 v[70:71], v77 offset0:10 offset1:11
	ds_read2_b32 v[72:73], v77 offset0:12 offset1:13
	ds_read2_b32 v[74:75], v77 offset0:14 offset1:15
	s_waitcnt lgkmcnt(0)
	v_add_f32_e32 v78, 0, v60
	v_add_f32_e32 v78, v78, v61
	v_add_f32_e32 v78, v78, v62
	v_add_f32_e32 v78, v78, v63
	v_add_f32_e32 v78, v78, v64
	v_add_f32_e32 v78, v78, v65
	v_add_f32_e32 v78, v78, v66
	v_add_f32_e32 v78, v78, v67
	v_add_f32_e32 v78, v78, v68
	v_add_f32_e32 v78, v78, v69
	v_add_f32_e32 v78, v78, v70
	v_add_f32_e32 v78, v78, v71
	v_add_f32_e32 v78, v78, v72
	v_add_f32_e32 v78, v78, v73
	v_add_f32_e32 v78, v78, v74
	v_add_f32_e32 v78, v78, v75
	s_nop 1
	v_add_f32_dpp v78, v78, v78 quad_perm:[1,0,3,2] row_mask:0xf bank_mask:0xf bound_ctrl:1
	s_nop 1
	v_add_f32_dpp v78, v78, v78 quad_perm:[2,3,0,1] row_mask:0xf bank_mask:0xf bound_ctrl:1
	v_lshlrev_b32_e32 v79, 4, v1
	ds_bpermute_b32 v78, v79, v78
	s_waitcnt lgkmcnt(0)
	s_barrier
	ds_read_b128 v[28:31], v53
	ds_read_b128 v[60:63], v56
	ds_read_b128 v[32:35], v53 offset:64
	ds_read_b128 v[64:67], v56 offset:64
	ds_read_b128 v[36:39], v53 offset:128
	ds_read_b128 v[68:71], v56 offset:128
	ds_read_b128 v[40:43], v53 offset:192
	ds_read_b128 v[72:75], v56 offset:192
	s_waitcnt lgkmcnt(6)
	v_mfma_f32_16x16x32_bf16 v[18:21], v[28:31], v[60:63], 0
	s_waitcnt lgkmcnt(4)
	v_mfma_f32_16x16x32_bf16 v[18:21], v[32:35], v[64:67], v[18:21]
	s_waitcnt lgkmcnt(2)
	v_mfma_f32_16x16x32_bf16 v[18:21], v[36:39], v[68:71], v[18:21]
	s_waitcnt lgkmcnt(0)
	v_mfma_f32_16x16x32_bf16 v[18:21], v[40:43], v[72:75], v[18:21]
	s_nop 7
	v_mul_f32_e32 v18, s44, v18
	v_mul_f32_e32 v19, s44, v19
	v_mul_f32_e32 v20, s44, v20
	v_mul_f32_e32 v21, s44, v21
	v_cvt_pk_bf16_f32 v18, v18, v18
	v_cvt_pk_bf16_f32 v19, v19, v19
	v_cvt_pk_bf16_f32 v20, v20, v20
	v_cvt_pk_bf16_f32 v21, v21, v21
	ds_write_b16 v55, v18
	ds_write_b16 v55, v19 offset:272
	ds_write_b16 v55, v20 offset:544
	ds_write_b16 v55, v21 offset:816
	s_waitcnt lgkmcnt(0)
	s_barrier
	ds_read_b128 v[28:31], v54
	ds_read_b128 v[60:63], v57
	ds_read_b128 v[32:35], v54 offset:64
	ds_read_b128 v[64:67], v57 offset:64
	ds_read_b128 v[36:39], v54 offset:128
	ds_read_b128 v[68:71], v57 offset:128
	ds_read_b128 v[40:43], v54 offset:192
	ds_read_b128 v[72:75], v57 offset:192
	s_waitcnt lgkmcnt(6)
	v_mfma_f32_16x16x32_bf16 v[18:21], v[28:31], v[60:63], 0
	s_waitcnt lgkmcnt(4)
	v_mfma_f32_16x16x32_bf16 v[18:21], v[32:35], v[64:67], v[18:21]
	s_waitcnt lgkmcnt(2)
	v_mfma_f32_16x16x32_bf16 v[18:21], v[36:39], v[68:71], v[18:21]
	s_waitcnt lgkmcnt(0)
	v_mfma_f32_16x16x32_bf16 v[18:21], v[40:43], v[72:75], v[18:21]
	s_nop 2
	v_mov_b32_e32 v28, v78
	s_load_dwordx2 s[4:5], s[0:1], 0x70
	v_lshl_or_b32 v30, v24, 2, s3
	v_ashrrev_i32_e32 v31, 31, v30
	v_mov_b32_e32 v107, 0
	s_waitcnt lgkmcnt(0)
	v_add_f32_e32 v34, v130, v28
	v_add_f32_e32 v35, v34, v18
	v_add_f32_e32 v28, v35, v35
	v_mul_f32_e32 v28, 0x3fb8aa3b, v28
	v_exp_f32_e32 v32, v28
	v_lshlrev_b64 v[28:29], 9, v[30:31]
	s_mov_b32 s8, 0x19200
	v_add3_u32 v37, v27, v25, s8
	v_add_f32_e32 v31, 1.0, v32
	v_rcp_f32_e32 v31, v31
	v_lshl_add_u64 v[32:33], s[4:5], 0, v[106:107]
	v_lshl_add_u64 v[28:29], v[32:33], 0, v[28:29]
	global_store_dword v[28:29], v35, off sc1
	v_fma_f32 v35, v31, -2.0, 1.0
	v_fma_f32 v28, -v35, v35, 1.0
	v_mul_f32_e32 v28, v129, v28
	v_add_f32_e32 v31, v34, v19
	v_cvt_pk_bf16_f32 v29, v28, s0
	v_mul_f32_e64 v27, v35, -v28
	v_add_f32_e32 v28, v31, v31
	v_mul_f32_e32 v28, 0x3fb8aa3b, v28
	v_exp_f32_e32 v38, v28
	v_cvt_pk_bf16_f32 v27, v27, s0
	ds_write_b16 v37, v27 offset:4352
	v_or_b32_e32 v28, 1, v30
	v_add_f32_e32 v27, 1.0, v38
	v_rcp_f32_e32 v27, v27
	ds_write_b16 v37, v29
	v_ashrrev_i32_e32 v29, 31, v28
	v_lshlrev_b64 v[28:29], 9, v[28:29]
	v_lshl_add_u64 v[28:29], v[32:33], 0, v[28:29]
	v_fma_f32 v27, v27, -2.0, 1.0
	global_store_dword v[28:29], v31, off sc1
	v_fma_f32 v28, -v27, v27, 1.0
	v_mul_f32_e32 v28, v129, v28
	v_cvt_pk_bf16_f32 v29, v28, s0
	v_add_f32_e32 v31, v34, v20
	ds_write_b16 v37, v29 offset:272
	v_add_f32_e32 v29, v31, v31
	v_mul_f32_e32 v29, 0x3fb8aa3b, v29
	v_exp_f32_e32 v38, v29
	v_mul_f32_e64 v28, v27, -v28
	v_cvt_pk_bf16_f32 v28, v28, s0
	ds_write_b16 v37, v28 offset:4624
	v_add_f32_e32 v38, 1.0, v38
	v_or_b32_e32 v28, 2, v30
	v_rcp_f32_e32 v38, v38
	v_ashrrev_i32_e32 v29, 31, v28
	v_lshlrev_b64 v[28:29], 9, v[28:29]
	v_lshl_add_u64 v[28:29], v[32:33], 0, v[28:29]
	global_store_dword v[28:29], v31, off sc1
	v_fma_f32 v28, v38, -2.0, 1.0
	v_fma_f32 v29, -v28, v28, 1.0
	v_mul_f32_e32 v29, v129, v29
	v_cvt_pk_bf16_f32 v31, v29, s0
	v_add_f32_e32 v34, v34, v21
	ds_write_b16 v37, v31 offset:544
	v_add_f32_e32 v31, v34, v34
	v_mul_f32_e32 v31, 0x3fb8aa3b, v31
	v_exp_f32_e32 v38, v31
	v_mul_f32_e64 v29, v28, -v29
	v_cvt_pk_bf16_f32 v29, v29, s0
	ds_write_b16 v37, v29 offset:4896
	v_add_f32_e32 v29, 1.0, v38
	v_rcp_f32_e32 v29, v29
	v_or_b32_e32 v30, 3, v30
	v_ashrrev_i32_e32 v31, 31, v30
	v_lshlrev_b64 v[30:31], 9, v[30:31]
	v_lshl_add_u64 v[30:31], v[32:33], 0, v[30:31]
	v_fma_f32 v29, v29, -2.0, 1.0
	global_store_dword v[30:31], v34, off sc1
	v_fma_f32 v30, -v29, v29, 1.0
	v_mul_f32_e32 v30, v129, v30
	v_cvt_pk_bf16_f32 v31, v30, s0
	v_mul_f32_e64 v30, v29, -v30
	v_cvt_pk_bf16_f32 v30, v30, s0
	ds_write_b16 v37, v30 offset:5168
	v_mov_b32_e32 v30, 0x1d800
	v_mul_f32_e32 v36, v129, v35
	v_lshl_or_b32 v32, v128, 6, v30
	v_mov_b32_e32 v30, v107
	ds_write_b16 v37, v31 offset:816
	v_mov_b32_e32 v31, 0
	v_mov_b32_dpp v30, v36 quad_perm:[1,0,3,2] row_mask:0xf bank_mask:0xf
	v_fmac_f32_e32 v30, v129, v35
	v_cmp_eq_u32_e32 vcc, 0, v1
	v_add_u32_e32 v26, v32, v26
	v_add_f32_dpp v30, v30, v30 quad_perm:[2,3,0,1] row_mask:0xf bank_mask:0xf bound_ctrl:1
	s_nop 1
	v_add_f32_dpp v30, v30, v30 row_half_mirror row_mask:0xf bank_mask:0xf bound_ctrl:1
	s_nop 1
	v_mov_b32_dpp v31, v30 row_mirror row_mask:0xf bank_mask:0xf
	s_and_saveexec_b64 s[4:5], vcc
	v_add_f32_e32 v30, v30, v31
	ds_write_b32 v26, v30
	s_or_b64 exec, exec, s[4:5]
	v_mul_f32_e32 v30, v129, v27
	v_mov_b32_e32 v31, 0
	s_nop 1
	v_mov_b32_dpp v31, v30 quad_perm:[1,0,3,2] row_mask:0xf bank_mask:0xf
	v_fmac_f32_e32 v31, v129, v27
	s_nop 1
	v_add_f32_dpp v27, v31, v31 quad_perm:[2,3,0,1] row_mask:0xf bank_mask:0xf bound_ctrl:1
	s_nop 1
	v_add_f32_dpp v27, v27, v27 row_half_mirror row_mask:0xf bank_mask:0xf bound_ctrl:1
	s_nop 1
	v_mov_b32_dpp v107, v27 row_mirror row_mask:0xf bank_mask:0xf
	s_and_saveexec_b64 s[4:5], vcc
	v_add_f32_e32 v27, v27, v107
	ds_write_b32 v26, v27 offset:4
	s_or_b64 exec, exec, s[4:5]
	v_mul_f32_e32 v30, v129, v28
	v_mov_b32_e32 v31, 0
	v_mov_b32_e32 v27, 0
	s_nop 0
	v_mov_b32_dpp v31, v30 quad_perm:[1,0,3,2] row_mask:0xf bank_mask:0xf
	v_fmac_f32_e32 v31, v129, v28
	v_mov_b32_e32 v30, 0
	s_nop 0
	v_add_f32_dpp v28, v31, v31 quad_perm:[2,3,0,1] row_mask:0xf bank_mask:0xf bound_ctrl:1
	s_nop 1
	v_add_f32_dpp v28, v28, v28 row_half_mirror row_mask:0xf bank_mask:0xf bound_ctrl:1
	s_nop 1
	v_mov_b32_dpp v30, v28 row_mirror row_mask:0xf bank_mask:0xf
	s_and_saveexec_b64 s[4:5], vcc
	v_add_f32_e32 v28, v28, v30
	ds_write_b32 v26, v28 offset:8
	s_or_b64 exec, exec, s[4:5]
	v_mul_f32_e32 v28, v129, v29
	v_mov_b32_e32 v30, 0
	s_nop 1
	v_mov_b32_dpp v30, v28 quad_perm:[1,0,3,2] row_mask:0xf bank_mask:0xf
	v_fmac_f32_e32 v30, v129, v29
	s_nop 1
	v_add_f32_dpp v28, v30, v30 quad_perm:[2,3,0,1] row_mask:0xf bank_mask:0xf bound_ctrl:1
	s_nop 1
	v_add_f32_dpp v28, v28, v28 row_half_mirror row_mask:0xf bank_mask:0xf bound_ctrl:1
	s_nop 1
	v_mov_b32_dpp v27, v28 row_mirror row_mask:0xf bank_mask:0xf
	s_and_saveexec_b64 s[4:5], vcc
	v_add_f32_e32 v27, v28, v27
	ds_write_b32 v26, v27 offset:12
	s_or_b64 exec, exec, s[4:5]
	s_mov_b64 s[4:5], 0
	s_branch .LBB0_28
.Lp_q:
	v_lshrrev_b32_e32 v122, 5, v0
	v_lshlrev_b32_e32 v122, 10, v122
	v_and_b32_e32 v125, 31, v0
	v_lshl_add_u32 v122, v125, 4, v122
	s_add_u32 s76, s38, 0x2000
	s_addc_u32 s77, s39, 0
	global_load_dwordx4 v[44:47], v120, s[76:77] nt
	s_and_b32 s13, s2, 7
	s_lshl_b32 s14, s13, 14
	v_add_u32_e32 v125, s14, v122
	global_load_dwordx4 v[132:135], v125, s[28:29]
	s_add_i32 s13, s2, 1
	s_and_b32 s13, s13, 7
	s_lshl_b32 s14, s13, 14
	v_add_u32_e32 v125, s14, v122
	global_load_dwordx4 v[136:139], v125, s[28:29]
	s_add_i32 s13, s2, 2
	s_and_b32 s13, s13, 7
	s_lshl_b32 s14, s13, 14
	v_add_u32_e32 v125, s14, v122
	global_load_dwordx4 v[140:143], v125, s[28:29]
	s_add_i32 s13, s2, 3
	s_and_b32 s13, s13, 7
	s_lshl_b32 s14, s13, 14
	v_add_u32_e32 v125, s14, v122
	global_load_dwordx4 v[144:147], v125, s[28:29]
	s_add_i32 s13, s2, 4
	s_and_b32 s13, s13, 7
	s_lshl_b32 s14, s13, 14
	v_add_u32_e32 v125, s14, v122
	global_load_dwordx4 v[148:151], v125, s[28:29]
	s_add_i32 s13, s2, 5
	s_and_b32 s13, s13, 7
	s_lshl_b32 s14, s13, 14
	v_add_u32_e32 v125, s14, v122
	global_load_dwordx4 v[152:155], v125, s[28:29]
	s_add_i32 s13, s2, 6
	s_and_b32 s13, s13, 7
	s_lshl_b32 s14, s13, 14
	v_add_u32_e32 v125, s14, v122
	global_load_dwordx4 v[156:159], v125, s[28:29]
	s_add_i32 s13, s2, 7
	s_and_b32 s13, s13, 7
	s_lshl_b32 s14, s13, 14
	v_add_u32_e32 v125, s14, v122
	global_load_dwordx4 v[160:163], v125, s[28:29]
	s_mov_b64 s[72:73], s[0:1]
	s_mov_b32 s74, s2
	s_mov_b32 s75, 0
	v_mov_b32_e32 v131, v0
	s_waitcnt vmcnt(19)
	v_cvt_pk_bf16_f32 v12, v2, v3
	v_cvt_pk_bf16_f32 v13, v4, v5
	ds_write_b64 v124, v[12:13]
	s_waitcnt vmcnt(18)
	v_cvt_pk_bf16_f32 v6, v80, v81
	v_cvt_pk_bf16_f32 v7, v82, v83
	s_and_b32 s13, s2, 7
	s_mul_i32 s14, s13, 0x1100
	v_add_u32_e32 v125, s14, v58
	ds_write_b64 v125, v[6:7]
	s_waitcnt vmcnt(17)
	v_cvt_pk_bf16_f32 v8, v84, v85
	v_cvt_pk_bf16_f32 v9, v86, v87
	s_add_i32 s13, s2, 1
	s_and_b32 s13, s13, 7
	s_mul_i32 s14, s13, 0x1100
	v_add_u32_e32 v10, s14, v58
	ds_write_b64 v10, v[8:9]
	s_waitcnt vmcnt(16)
	v_cvt_pk_bf16_f32 v6, v88, v89
	v_cvt_pk_bf16_f32 v7, v90, v91
	s_add_i32 s13, s2, 2
	s_and_b32 s13, s13, 7
	s_mul_i32 s14, s13, 0x1100
	v_add_u32_e32 v125, s14, v58
	ds_write_b64 v125, v[6:7]
	s_waitcnt vmcnt(15)
	v_cvt_pk_bf16_f32 v8, v92, v93
	v_cvt_pk_bf16_f32 v9, v94, v95
	s_add_i32 s13, s2, 3
	s_and_b32 s13, s13, 7
	s_mul_i32 s14, s13, 0x1100
	v_add_u32_e32 v10, s14, v58
	ds_write_b64 v10, v[8:9]
	s_waitcnt vmcnt(14)
	v_cvt_pk_bf16_f32 v6, v96, v97
	v_cvt_pk_bf16_f32 v7, v98, v99
	s_add_i32 s13, s2, 4
	s_and_b32 s13, s13, 7
	s_mul_i32 s14, s13, 0x1100
	v_add_u32_e32 v125, s14, v58
	ds_write_b64 v125, v[6:7]
	s_waitcnt vmcnt(13)
	v_cvt_pk_bf16_f32 v8, v100, v101
	v_cvt_pk_bf16_f32 v9, v102, v103
	s_add_i32 s13, s2, 5
	s_and_b32 s13, s13, 7
	s_mul_i32 s14, s13, 0x1100
	v_add_u32_e32 v10, s14, v58
	ds_write_b64 v10, v[8:9]
	s_waitcnt vmcnt(12)
	v_cvt_pk_bf16_f32 v6, v108, v109
	v_cvt_pk_bf16_f32 v7, v110, v111
	s_add_i32 s13, s2, 6
	s_and_b32 s13, s13, 7
	s_mul_i32 s14, s13, 0x1100
	v_add_u32_e32 v125, s14, v58
	ds_write_b64 v125, v[6:7]
	s_waitcnt vmcnt(11)
	v_cvt_pk_bf16_f32 v8, v112, v113
	v_cvt_pk_bf16_f32 v9, v114, v115
	s_add_i32 s13, s2, 7
	s_and_b32 s13, s13, 7
	s_mul_i32 s14, s13, 0x1100
	v_add_u32_e32 v10, s14, v58
	ds_write_b64 v10, v[8:9]
	s_waitcnt vmcnt(7)
	v_cvt_pk_bf16_f32 v6, v132, v133
	v_cvt_pk_bf16_f32 v7, v134, v135
	s_and_b32 s13, s2, 7
	s_mul_i32 s14, s13, 0x1100
	s_add_i32 s14, s14, 34816
	v_add_u32_e32 v125, s14, v58
	ds_write_b64 v125, v[6:7]
	s_waitcnt vmcnt(6)
	v_cvt_pk_bf16_f32 v8, v136, v137
	v_cvt_pk_bf16_f32 v9, v138, v139
	s_add_i32 s13, s2, 1
	s_and_b32 s13, s13, 7
	s_mul_i32 s14, s13, 0x1100
	s_add_i32 s14, s14, 34816
	v_add_u32_e32 v10, s14, v58
	ds_write_b64 v10, v[8:9]
	s_waitcnt vmcnt(5)
	v_cvt_pk_bf16_f32 v6, v140, v141
	v_cvt_pk_bf16_f32 v7, v142, v143
	s_add_i32 s13, s2, 2
	s_and_b32 s13, s13, 7
	s_mul_i32 s14, s13, 0x1100
	s_add_i32 s14, s14, 34816
	v_add_u32_e32 v125, s14, v58
	ds_write_b64 v125, v[6:7]
	s_waitcnt vmcnt(4)
	v_cvt_pk_bf16_f32 v8, v144, v145
	v_cvt_pk_bf16_f32 v9, v146, v147
	s_add_i32 s13, s2, 3
	s_and_b32 s13, s13, 7
	s_mul_i32 s14, s13, 0x1100
	s_add_i32 s14, s14, 34816
	v_add_u32_e32 v10, s14, v58
	ds_write_b64 v10, v[8:9]
	s_waitcnt vmcnt(3)
	v_cvt_pk_bf16_f32 v6, v148, v149
	v_cvt_pk_bf16_f32 v7, v150, v151
	s_add_i32 s13, s2, 4
	s_and_b32 s13, s13, 7
	s_mul_i32 s14, s13, 0x1100
	s_add_i32 s14, s14, 34816
	v_add_u32_e32 v125, s14, v58
	ds_write_b64 v125, v[6:7]
	s_waitcnt vmcnt(2)
	v_cvt_pk_bf16_f32 v8, v152, v153
	v_cvt_pk_bf16_f32 v9, v154, v155
	s_add_i32 s13, s2, 5
	s_and_b32 s13, s13, 7
	s_mul_i32 s14, s13, 0x1100
	s_add_i32 s14, s14, 34816
	v_add_u32_e32 v10, s14, v58
	ds_write_b64 v10, v[8:9]
	s_waitcnt vmcnt(1)
	v_cvt_pk_bf16_f32 v6, v156, v157
	v_cvt_pk_bf16_f32 v7, v158, v159
	s_add_i32 s13, s2, 6
	s_and_b32 s13, s13, 7
	s_mul_i32 s14, s13, 0x1100
	s_add_i32 s14, s14, 34816
	v_add_u32_e32 v125, s14, v58
	ds_write_b64 v125, v[6:7]
	s_waitcnt vmcnt(0)
	v_cvt_pk_bf16_f32 v8, v160, v161
	v_cvt_pk_bf16_f32 v9, v162, v163
	s_add_i32 s13, s2, 7
	s_and_b32 s13, s13, 7
	s_mul_i32 s14, s13, 0x1100
	s_add_i32 s14, s14, 34816
	v_add_u32_e32 v10, s14, v58
	ds_write_b64 v10, v[8:9]
	s_lshl_b32 s2, s74, 1
.Lq_tile:
	s_lshl_b32 s12, s2, 4
	s_waitcnt lgkmcnt(0)
	s_barrier
	ds_read_b128 v[28:31], v53
	ds_read_b128 v[60:63], v56
	ds_read_b128 v[32:35], v53 offset:64
	ds_read_b128 v[64:67], v56 offset:64
	ds_read_b128 v[36:39], v53 offset:128
	ds_read_b128 v[68:71], v56 offset:128
	ds_read_b128 v[40:43], v53 offset:192
	ds_read_b128 v[72:75], v56 offset:192
	s_waitcnt lgkmcnt(6)
	v_mfma_f32_16x16x32_bf16 v[18:21], v[28:31], v[60:63], 0
	s_waitcnt lgkmcnt(4)
	v_mfma_f32_16x16x32_bf16 v[18:21], v[32:35], v[64:67], v[18:21]
	s_waitcnt lgkmcnt(2)
	v_mfma_f32_16x16x32_bf16 v[18:21], v[36:39], v[68:71], v[18:21]
	s_waitcnt lgkmcnt(0)
	v_mfma_f32_16x16x32_bf16 v[18:21], v[40:43], v[72:75], v[18:21]
	s_nop 7
	v_mul_f32_e32 v18, s44, v18
	v_mul_f32_e32 v19, s44, v19
	v_mul_f32_e32 v20, s44, v20
	v_mul_f32_e32 v21, s44, v21
	v_cvt_pk_bf16_f32 v18, v18, v18
	v_cvt_pk_bf16_f32 v19, v19, v19
	v_cvt_pk_bf16_f32 v20, v20, v20
	v_cvt_pk_bf16_f32 v21, v21, v21
	ds_write_b16 v55, v18
	ds_write_b16 v55, v19 offset:272
	ds_write_b16 v55, v20 offset:544
	ds_write_b16 v55, v21 offset:816
	s_waitcnt lgkmcnt(0)
	s_barrier
	ds_read_b128 v[28:31], v54
	ds_read_b128 v[60:63], v57
	ds_read_b128 v[32:35], v54 offset:64
	ds_read_b128 v[64:67], v57 offset:64
	ds_read_b128 v[36:39], v54 offset:128
	ds_read_b128 v[68:71], v57 offset:128
	ds_read_b128 v[40:43], v54 offset:192
	ds_read_b128 v[72:75], v57 offset:192
	s_waitcnt lgkmcnt(6)
	v_mfma_f32_16x16x32_bf16 v[18:21], v[28:31], v[60:63], 0
	s_waitcnt lgkmcnt(4)
	v_mfma_f32_16x16x32_bf16 v[18:21], v[32:35], v[64:67], v[18:21]
	s_waitcnt lgkmcnt(2)
	v_mfma_f32_16x16x32_bf16 v[18:21], v[36:39], v[68:71], v[18:21]
	s_waitcnt lgkmcnt(0)
	v_mfma_f32_16x16x32_bf16 v[18:21], v[40:43], v[72:75], v[18:21]
	s_load_dwordx2 s[4:5], s[0:1], 0x68
	v_lshl_or_b32 v26, v24, 2, s12
	v_mov_b32_e32 v107, 0
	v_ashrrev_i32_e32 v27, 31, v26
	v_lshlrev_b64 v[28:29], 9, v[26:27]
	s_waitcnt lgkmcnt(0)
	v_lshl_add_u64 v[30:31], s[4:5], 0, v[106:107]
	v_lshl_add_u64 v[28:29], v[30:31], 0, v[28:29]
	v_mul_u32_u24_e32 v24, 0x440, v24
	s_mov_b32 s4, 0x19200
	global_store_dword v[28:29], v18, off sc1
	v_add3_u32 v28, v24, v25, s4
	v_mul_f32_e32 v24, v18, v18
	v_cvt_pk_bf16_f32 v27, v18, s0
	v_cvt_pk_bf16_f32 v24, v24, s0
	ds_write_b16 v28, v27
	ds_write_b16 v28, v24 offset:4352
	v_max3_f32 v27, |v18|, 0, |v19|
	v_or_b32_e32 v24, 1, v26
	v_cvt_pk_bf16_f32 v18, v19, s0
	v_ashrrev_i32_e32 v25, 31, v24
	ds_write_b16 v28, v18 offset:272
	v_mul_f32_e32 v18, v19, v19
	v_lshlrev_b64 v[24:25], 9, v[24:25]
	v_cvt_pk_bf16_f32 v18, v18, s0
	v_lshl_add_u64 v[24:25], v[30:31], 0, v[24:25]
	ds_write_b16 v28, v18 offset:4624
	v_or_b32_e32 v18, 2, v26
	global_store_dword v[24:25], v19, off sc1
	v_ashrrev_i32_e32 v19, 31, v18
	v_lshlrev_b64 v[18:19], 9, v[18:19]
	v_lshl_add_u64 v[18:19], v[30:31], 0, v[18:19]
	global_store_dword v[18:19], v20, off sc1
	v_cvt_pk_bf16_f32 v18, v20, s0
	ds_write_b16 v28, v18 offset:544
	v_mul_f32_e32 v18, v20, v20
	v_cvt_pk_bf16_f32 v18, v18, s0
	ds_write_b16 v28, v18 offset:4896
	v_or_b32_e32 v18, 3, v26
	v_ashrrev_i32_e32 v19, 31, v18
	v_lshlrev_b64 v[18:19], 9, v[18:19]
	v_lshl_add_u64 v[18:19], v[30:31], 0, v[18:19]
	global_store_dword v[18:19], v21, off sc1
	v_cvt_pk_bf16_f32 v18, v21, s0
	ds_write_b16 v28, v18 offset:816
	v_mul_f32_e32 v18, v21, v21
	v_cvt_pk_bf16_f32 v18, v18, s0
	v_max3_f32 v20, v27, |v20|, |v21|
	ds_write_b16 v28, v18 offset:5168
	v_mov_b32_e32 v18, v107
	v_mov_b32_e32 v19, v107
	v_cmp_eq_u32_e32 vcc, 0, v126
	v_mov_b32_dpp v18, v20 quad_perm:[1,0,3,2] row_mask:0xf bank_mask:0xf
	v_max_f32_e32 v18, v18, v18
	v_max_f32_e32 v18, v20, v18
	s_nop 1
	v_mov_b32_dpp v19, v18 quad_perm:[2,3,0,1] row_mask:0xf bank_mask:0xf
	v_max_f32_e32 v19, v19, v19
	v_max_f32_e32 v18, v18, v19
	v_mov_b32_e32 v19, v107
	s_nop 1
	v_mov_b32_dpp v19, v18 row_half_mirror row_mask:0xf bank_mask:0xf
	v_max_f32_e32 v19, v19, v19
	v_max_f32_e32 v18, v18, v19
	v_mov_b32_e32 v19, v107
	s_nop 1
	v_mov_b32_dpp v19, v18 row_mirror row_mask:0xf bank_mask:0xf
	v_max_f32_e32 v19, v19, v19
	v_max_f32_e32 v18, v18, v19
	s_nop 0
	v_readlane_b32 s8, v18, 0
	v_readlane_b32 s9, v18, 16
	v_readlane_b32 s10, v18, 32
	v_readlane_b32 s11, v18, 48
	v_and_b32_e32 v18, 0x7fffffff, v129
	s_nop 1
	v_add_f32_dpp v18, v18, |v129| quad_perm:[1,0,3,2] row_mask:0xf bank_mask:0xf bound_ctrl:1
	s_nop 1
	v_add_f32_dpp v18, v18, v18 quad_perm:[2,3,0,1] row_mask:0xf bank_mask:0xf bound_ctrl:1
	s_nop 1
	v_add_f32_dpp v18, v18, v18 row_half_mirror row_mask:0xf bank_mask:0xf bound_ctrl:1
	s_nop 1
	v_mov_b32_dpp v107, v18 row_mirror row_mask:0xf bank_mask:0xf
	s_and_saveexec_b64 s[4:5], vcc
	s_cbranch_execz .Lq_27
	v_mov_b32_e32 v19, 0x1d800
	v_lshl_or_b32 v20, v128, 6, v19
	v_add_f32_e32 v19, v18, v107
	v_max_f32_e64 v18, s11, s11
	v_max_f32_e64 v21, s10, s10
	v_max_f32_e32 v18, v21, v18
	v_mov_b32_e32 v21, s9
	v_max3_f32 v18, s8, v21, v18
	ds_write_b64 v20, v[18:19]
.Lq_27:
	s_or_b64 exec, exec, s[4:5]
	s_waitcnt lgkmcnt(0)
	s_barrier
	v_cmp_eq_u32_e32 vcc, 0, v0
	s_and_saveexec_b64 s[6:7], vcc
	s_cbranch_execz .Lq_37
	v_mov_b32_e32 v18, 0x1d800
	v_mov_b32_e32 v20, 0x1d840
	ds_read_b64 v[18:19], v18
	ds_read_b64 v[20:21], v20
	v_mov_b32_e32 v24, 0x1d880
	v_mov_b32_e32 v26, 0x1d8c0
	ds_read_b64 v[24:25], v24
	ds_read_b64 v[26:27], v26
	s_waitcnt lgkmcnt(0)
	v_max_f32_e32 v18, v18, v18
	v_max_f32_e32 v20, v20, v20
	v_max_f32_e32 v18, v18, v20
	v_add_f32_e32 v19, v19, v21
	v_add_f32_e32 v19, v19, v25
	v_max3_f32 v21, v18, v24, v26
	v_mov_b32_e32 v18, 0x1d900
	v_add_f32_e32 v30, v19, v27
	v_mov_b32_e32 v19, 0x1d940
	v_mov_b32_e32 v20, 0x1d980
	ds_read_b64 v[24:25], v18
	ds_read_b64 v[26:27], v19
	ds_read_b64 v[28:29], v20
	v_mov_b32_e32 v18, 0x1d9c0
	ds_read_b96 v[18:20], v18
	s_mov_b32 s10, 0x3b800000
	s_waitcnt lgkmcnt(2)
	v_max3_f32 v21, v21, v24, v26
	s_waitcnt lgkmcnt(0)
	v_add_f32_e32 v20, v30, v25
	s_mov_b32 s11, 0x3eaab368
	v_max3_f32 v24, v21, v28, v18
	v_mul_f32_e32 v25, v24, v24
	v_add_f32_e32 v20, v20, v27
	v_pk_mul_f32 v[26:27], v[24:25], s[10:11]
	v_add_f32_e32 v20, v20, v29
	v_mov_b32_e32 v28, v26
	v_mul_f32_e32 v21, 0x3ec51eb8, v25
	v_mov_b32_e32 v18, v19
	v_mov_b32_e32 v19, v26
	v_fmac_f32_e32 v28, v24, v27
	v_pk_add_f32 v[18:19], v[20:21], v[18:19]
	s_mov_b32 s3, 0x3a83126f
	v_mul_f32_e32 v20, v18, v28
	s_load_dwordx2 s[8:9], s[0:1], 0x78
	v_cmp_nge_f32_e32 vcc, s3, v20
	v_mul_f32_e32 v18, v18, v19
	s_and_b64 s[10:11], vcc, exec
	v_cmp_nge_f32_e32 vcc, s3, v18
	s_cselect_b32 s12, 3, 2
	s_and_b64 s[10:11], vcc, exec
	s_cselect_b32 s12, s12, 1
	s_ashr_i32 s3, s2, 31
	s_lshl_b64 s[10:11], s[2:3], 2
	s_waitcnt lgkmcnt(0)
	s_add_u32 s8, s8, s10
	s_addc_u32 s9, s9, s11
	v_mov_b32_e32 v18, 0
	v_mov_b32_e32 v19, s12
	global_store_dword v18, v19, s[8:9] sc1

.Lq_39:
	s_or_b64 exec, exec, s[6:7]
	s_cmp_lg_u32 s75, 0
	s_cbranch_scc1 .Lq_done
	s_mov_b32 s75, 1
	s_add_i32 s2, s2, 1
	s_mov_b64 s[0:1], s[72:73]
	v_mov_b32_e32 v0, v131
	v_and_b32_e32 v1, 15, v0
	v_bfe_u32 v24, v0, 4, 2
	v_lshl_or_b32 v107, v128, 4, v1
	v_lshlrev_b32_e32 v25, 1, v107
	v_and_b32_e32 v26, 48, v0
	v_mul_u32_u24_e32 v27, 0x440, v24
	v_cvt_pk_bf16_f32 v12, v44, v45
	v_cvt_pk_bf16_f32 v13, v46, v47
	ds_write_b64 v124, v[12:13]
	s_branch .Lq_tile

.Lp_mask:
	s_lshl_b32 s13, s13, 5
	v_lshl_add_u32 v20, v128, 2, s13
	v_lshlrev_b32_e32 v21, 12, v20
	v_lshl_add_u32 v21, v126, 4, v21
	v_add_u32_e32 v22, 0x1000, v21
	v_add_u32_e32 v23, 0x2000, v21
	v_add_u32_e32 v24, 0x3000, v21
	global_load_dwordx4 v[132:135], v21, s[34:35] nt
	global_load_dwordx4 v[136:139], v21, s[34:35] offset:1024 nt
	global_load_dwordx4 v[140:143], v21, s[34:35] offset:2048 nt
	global_load_dwordx4 v[144:147], v21, s[34:35] offset:3072 nt
	global_load_dwordx4 v[148:151], v22, s[34:35] nt
	global_load_dwordx4 v[152:155], v22, s[34:35] offset:1024 nt
	global_load_dwordx4 v[156:159], v22, s[34:35] offset:2048 nt
	global_load_dwordx4 v[160:163], v22, s[34:35] offset:3072 nt
	global_load_dwordx4 v[164:167], v23, s[34:35] nt
	global_load_dwordx4 v[168:171], v23, s[34:35] offset:1024 nt
	global_load_dwordx4 v[172:175], v23, s[34:35] offset:2048 nt
	global_load_dwordx4 v[176:179], v23, s[34:35] offset:3072 nt
	global_load_dwordx4 v[180:183], v24, s[34:35] nt
	global_load_dwordx4 v[184:187], v24, s[34:35] offset:1024 nt
	global_load_dwordx4 v[188:191], v24, s[34:35] offset:2048 nt
	global_load_dwordx4 v[192:195], v24, s[34:35] offset:3072 nt
	s_waitcnt vmcnt(12)
	v_mov_b32_e32 v44, 0
	v_cmp_ne_u32_e64 s[46:47], 0, v147
	v_cmp_ne_u32_e64 s[48:49], 0, v146
	v_cmp_ne_u32_e64 s[50:51], 0, v145
	v_cmp_ne_u32_e64 s[52:53], 0, v144
	v_addc_co_u32_e64 v44, s[54:55], v44, v44, s[46:47]
	v_addc_co_u32_e64 v44, s[54:55], v44, v44, s[48:49]
	v_addc_co_u32_e64 v44, s[54:55], v44, v44, s[50:51]
	v_addc_co_u32_e64 v44, s[54:55], v44, v44, s[52:53]
	v_cmp_ne_u32_e64 s[46:47], 0, v143
	v_cmp_ne_u32_e64 s[48:49], 0, v142
	v_cmp_ne_u32_e64 s[50:51], 0, v141
	v_cmp_ne_u32_e64 s[52:53], 0, v140
	v_addc_co_u32_e64 v44, s[54:55], v44, v44, s[46:47]
	v_addc_co_u32_e64 v44, s[54:55], v44, v44, s[48:49]
	v_addc_co_u32_e64 v44, s[54:55], v44, v44, s[50:51]
	v_addc_co_u32_e64 v44, s[54:55], v44, v44, s[52:53]
	v_cmp_ne_u32_e64 s[46:47], 0, v139
	v_cmp_ne_u32_e64 s[48:49], 0, v138
	v_cmp_ne_u32_e64 s[50:51], 0, v137
	v_cmp_ne_u32_e64 s[52:53], 0, v136
	v_addc_co_u32_e64 v44, s[54:55], v44, v44, s[46:47]
	v_addc_co_u32_e64 v44, s[54:55], v44, v44, s[48:49]
	v_addc_co_u32_e64 v44, s[54:55], v44, v44, s[50:51]
	v_addc_co_u32_e64 v44, s[54:55], v44, v44, s[52:53]
	v_cmp_ne_u32_e64 s[46:47], 0, v135
	v_cmp_ne_u32_e64 s[48:49], 0, v134
	v_cmp_ne_u32_e64 s[50:51], 0, v133
	v_cmp_ne_u32_e64 s[52:53], 0, v132
	v_addc_co_u32_e64 v44, s[54:55], v44, v44, s[46:47]
	v_addc_co_u32_e64 v44, s[54:55], v44, v44, s[48:49]
	v_addc_co_u32_e64 v44, s[54:55], v44, v44, s[50:51]
	v_addc_co_u32_e64 v44, s[54:55], v44, v44, s[52:53]
	s_waitcnt vmcnt(8)
	v_mov_b32_e32 v45, 0
	v_cmp_ne_u32_e64 s[46:47], 0, v163
	v_cmp_ne_u32_e64 s[48:49], 0, v162
	v_cmp_ne_u32_e64 s[50:51], 0, v161
	v_cmp_ne_u32_e64 s[52:53], 0, v160
	v_addc_co_u32_e64 v45, s[54:55], v45, v45, s[46:47]
	v_addc_co_u32_e64 v45, s[54:55], v45, v45, s[48:49]
	v_addc_co_u32_e64 v45, s[54:55], v45, v45, s[50:51]
	v_addc_co_u32_e64 v45, s[54:55], v45, v45, s[52:53]
	v_cmp_ne_u32_e64 s[46:47], 0, v159
	v_cmp_ne_u32_e64 s[48:49], 0, v158
	v_cmp_ne_u32_e64 s[50:51], 0, v157
	v_cmp_ne_u32_e64 s[52:53], 0, v156
	v_addc_co_u32_e64 v45, s[54:55], v45, v45, s[46:47]
	v_addc_co_u32_e64 v45, s[54:55], v45, v45, s[48:49]
	v_addc_co_u32_e64 v45, s[54:55], v45, v45, s[50:51]
	v_addc_co_u32_e64 v45, s[54:55], v45, v45, s[52:53]
	v_cmp_ne_u32_e64 s[46:47], 0, v155
	v_cmp_ne_u32_e64 s[48:49], 0, v154
	v_cmp_ne_u32_e64 s[50:51], 0, v153
	v_cmp_ne_u32_e64 s[52:53], 0, v152
	v_addc_co_u32_e64 v45, s[54:55], v45, v45, s[46:47]
	v_addc_co_u32_e64 v45, s[54:55], v45, v45, s[48:49]
	v_addc_co_u32_e64 v45, s[54:55], v45, v45, s[50:51]
	v_addc_co_u32_e64 v45, s[54:55], v45, v45, s[52:53]
	v_cmp_ne_u32_e64 s[46:47], 0, v151
	v_cmp_ne_u32_e64 s[48:49], 0, v150
	v_cmp_ne_u32_e64 s[50:51], 0, v149
	v_cmp_ne_u32_e64 s[52:53], 0, v148
	v_addc_co_u32_e64 v45, s[54:55], v45, v45, s[46:47]
	v_addc_co_u32_e64 v45, s[54:55], v45, v45, s[48:49]
	v_addc_co_u32_e64 v45, s[54:55], v45, v45, s[50:51]
	v_addc_co_u32_e64 v45, s[54:55], v45, v45, s[52:53]
	s_waitcnt vmcnt(4)
	v_mov_b32_e32 v46, 0
	v_cmp_ne_u32_e64 s[46:47], 0, v179
	v_cmp_ne_u32_e64 s[48:49], 0, v178
	v_cmp_ne_u32_e64 s[50:51], 0, v177
	v_cmp_ne_u32_e64 s[52:53], 0, v176
	v_addc_co_u32_e64 v46, s[54:55], v46, v46, s[46:47]
	v_addc_co_u32_e64 v46, s[54:55], v46, v46, s[48:49]
	v_addc_co_u32_e64 v46, s[54:55], v46, v46, s[50:51]
	v_addc_co_u32_e64 v46, s[54:55], v46, v46, s[52:53]
	v_cmp_ne_u32_e64 s[46:47], 0, v175
	v_cmp_ne_u32_e64 s[48:49], 0, v174
	v_cmp_ne_u32_e64 s[50:51], 0, v173
	v_cmp_ne_u32_e64 s[52:53], 0, v172
	v_addc_co_u32_e64 v46, s[54:55], v46, v46, s[46:47]
	v_addc_co_u32_e64 v46, s[54:55], v46, v46, s[48:49]
	v_addc_co_u32_e64 v46, s[54:55], v46, v46, s[50:51]
	v_addc_co_u32_e64 v46, s[54:55], v46, v46, s[52:53]
	v_cmp_ne_u32_e64 s[46:47], 0, v171
	v_cmp_ne_u32_e64 s[48:49], 0, v170
	v_cmp_ne_u32_e64 s[50:51], 0, v169
	v_cmp_ne_u32_e64 s[52:53], 0, v168
	v_addc_co_u32_e64 v46, s[54:55], v46, v46, s[46:47]
	v_addc_co_u32_e64 v46, s[54:55], v46, v46, s[48:49]
	v_addc_co_u32_e64 v46, s[54:55], v46, v46, s[50:51]
	v_addc_co_u32_e64 v46, s[54:55], v46, v46, s[52:53]
	v_cmp_ne_u32_e64 s[46:47], 0, v167
	v_cmp_ne_u32_e64 s[48:49], 0, v166
	v_cmp_ne_u32_e64 s[50:51], 0, v165
	v_cmp_ne_u32_e64 s[52:53], 0, v164
	v_addc_co_u32_e64 v46, s[54:55], v46, v46, s[46:47]
	v_addc_co_u32_e64 v46, s[54:55], v46, v46, s[48:49]
	v_addc_co_u32_e64 v46, s[54:55], v46, v46, s[50:51]
	v_addc_co_u32_e64 v46, s[54:55], v46, v46, s[52:53]
	s_waitcnt vmcnt(0)
	v_mov_b32_e32 v47, 0
	v_cmp_ne_u32_e64 s[46:47], 0, v195
	v_cmp_ne_u32_e64 s[48:49], 0, v194
	v_cmp_ne_u32_e64 s[50:51], 0, v193
	v_cmp_ne_u32_e64 s[52:53], 0, v192
	v_addc_co_u32_e64 v47, s[54:55], v47, v47, s[46:47]
	v_addc_co_u32_e64 v47, s[54:55], v47, v47, s[48:49]
	v_addc_co_u32_e64 v47, s[54:55], v47, v47, s[50:51]
	v_addc_co_u32_e64 v47, s[54:55], v47, v47, s[52:53]
	v_cmp_ne_u32_e64 s[46:47], 0, v191
	v_cmp_ne_u32_e64 s[48:49], 0, v190
	v_cmp_ne_u32_e64 s[50:51], 0, v189
	v_cmp_ne_u32_e64 s[52:53], 0, v188
	v_addc_co_u32_e64 v47, s[54:55], v47, v47, s[46:47]
	v_addc_co_u32_e64 v47, s[54:55], v47, v47, s[48:49]
	v_addc_co_u32_e64 v47, s[54:55], v47, v47, s[50:51]
	v_addc_co_u32_e64 v47, s[54:55], v47, v47, s[52:53]
	v_cmp_ne_u32_e64 s[46:47], 0, v187
	v_cmp_ne_u32_e64 s[48:49], 0, v186
	v_cmp_ne_u32_e64 s[50:51], 0, v185
	v_cmp_ne_u32_e64 s[52:53], 0, v184
	v_addc_co_u32_e64 v47, s[54:55], v47, v47, s[46:47]
	v_addc_co_u32_e64 v47, s[54:55], v47, v47, s[48:49]
	v_addc_co_u32_e64 v47, s[54:55], v47, v47, s[50:51]
	v_addc_co_u32_e64 v47, s[54:55], v47, v47, s[52:53]
	v_cmp_ne_u32_e64 s[46:47], 0, v183
	v_cmp_ne_u32_e64 s[48:49], 0, v182
	v_cmp_ne_u32_e64 s[50:51], 0, v181
	v_cmp_ne_u32_e64 s[52:53], 0, v180
	v_addc_co_u32_e64 v47, s[54:55], v47, v47, s[46:47]
	v_addc_co_u32_e64 v47, s[54:55], v47, v47, s[48:49]
	v_addc_co_u32_e64 v47, s[54:55], v47, v47, s[50:51]
	v_addc_co_u32_e64 v47, s[54:55], v47, v47, s[52:53]
	v_lshlrev_b32_e32 v28, 7, v20
	v_lshl_add_u32 v28, v126, 1, v28
	global_store_short v28, v44, s[36:37] sc1
	global_store_short v28, v45, s[36:37] offset:128 sc1
	global_store_short v28, v46, s[36:37] offset:256 sc1
	global_store_short v28, v47, s[36:37] offset:384 sc1
	s_endpgm
